# router phase: second W1-conversion slice in every 16-token group (experts 12..15 staged in spare VGPRs), stand-alone conversion stops at expert 11 on the 256-WG grid
# baseline (speedup 1.0000x reference)
.LBB0_215:
	s_cmp_lt_i32 s4, 3
	s_waitcnt lgkmcnt(0)
	s_cselect_b64 s[0:1], -1, 0
	s_cmp_gt_i32 s5, 2
	s_cselect_b64 s[2:3], -1, 0
	s_and_b64 s[0:1], s[0:1], s[2:3]
	s_andn2_b64 vcc, exec, s[0:1]
	s_cbranch_vccnz .LBB0_347
	v_readlane_b32 s18, v254, 11
	s_load_dword s6, s[52:53], 0xd0
	s_load_dwordx2 s[4:5], s[52:53], 0xc0
	s_bitcmp0_b32 s18, 0
	s_cselect_b64 s[0:1], -1, 0
	s_bitcmp1_b32 s18, 0
	v_readlane_b32 s8, v254, 10
	s_cselect_b64 s[10:11], -1, 0
	s_lshl_b32 s2, s8, 14
	s_add_i32 s36, s2, 0
	s_lshl_b32 s2, s18, 2
	s_add_i32 s37, s2, s8
	s_waitcnt lgkmcnt(0)
	s_lshl_b32 s2, s6, 2
	s_add_i32 s2, s2, 4
	s_and_b32 s38, s2, -8
	s_cmpk_lt_i32 s37, 0x1400
	s_cselect_b64 s[2:3], -1, 0
	s_add_u32 s39, s4, 0x2000000
	s_addc_u32 s40, s5, 0
	s_lshl_b32 s4, s18, 3
	s_add_i32 s57, s8, s4
	s_lshl_b32 s41, s6, 3
	s_addk_i32 s57, 0x1400
	s_movk_i32 s32, 0x4c00
	s_cmpk_eq_i32 s99, 0x100
	s_cselect_b32 s32, 0x3000, s32
	s_cmp_lt_i32 s57, s32
	s_cselect_b64 s[14:15], -1, 0
	s_lshl_b32 s4, s50, 3
	s_bfe_u32 s6, s61, 0x20006
	s_lshr_b32 s7, s61, 8
	s_add_i32 s59, s8, s4
	s_add_i32 s5, s41, 0x2fff
	s_mov_b32 s20, s61
	s_lshl_b32 s61, s8, 10
	s_lshl_b32 s63, s7, 6
	s_lshl_b32 s65, s7, 13
	s_lshl_b32 s67, s6, 12
	s_cmpk_lt_i32 s18, 0x600
	s_cselect_b64 s[16:17], -1, 0
	s_ashr_i32 s4, s18, 31
	s_lshr_b32 s4, s4, 29
	s_add_i32 s4, s18, s4
	s_ashr_i32 s8, s4, 3
	s_and_b32 s4, s4, -8
	s_sub_i32 s4, s18, s4
	s_cmp_lt_i32 s4, 0
	s_movk_i32 s69, 0xc1
	s_cselect_b32 s18, s69, 0xc0
	s_mul_i32 s4, s18, s4
	s_add_i32 s4, s4, s8
	s_mul_hi_i32 s8, s4, 0x2aaaaaab
	s_lshr_b32 s18, s8, 31
	s_ashr_i32 s8, s8, 4
	s_add_i32 s8, s8, s18
	s_lshl_b32 s82, s8, 3
	s_mulk_i32 s8, 0x60
	s_sub_i32 s8, s4, s8
	s_bfe_i32 s4, s8, 0x80000
	s_bfe_u32 s4, s4, 0x3000c
	s_add_i32 s18, s8, s4
	s_bfe_i32 s4, s18, 0x80000
	s_and_b32 s18, s18, 0xf8
	s_sub_i32 s8, s8, s18
	s_sext_i32_i16 s19, s4
	s_sext_i32_i8 s8, s8
	s_lshr_b32 s4, s19, 3
	s_add_i32 s82, s82, s8
	s_ashr_i32 s44, s19, 3
	s_cmp_eq_u32 s7, 1
	s_cselect_b64 s[18:19], -1, 0
	s_cmpk_lt_u32 s20, 0x100
	s_cselect_b64 s[20:21], -1, 0
	s_and_b64 s[22:23], s[0:1], s[2:3]
	s_abs_i32 s2, s41
	v_cvt_f32_u32_e32 v0, s2
	s_bfe_i64 s[0:1], s[4:5], 0x100000
	s_sub_i32 s3, 0, s2
	s_lshl_b64 s[26:27], s[0:1], 20
	v_rcp_iflag_f32_e32 v0, v0
	s_abs_i32 s1, s5
	s_lshl_b32 s86, s82, 8
	s_xor_b32 s0, s5, s41
	v_mul_f32_e32 v0, 0x4f7ffffe, v0
	v_cvt_u32_f32_e32 v0, v0
	s_lshl_b32 s84, s6, 6
	s_lshl_b32 s85, s82, 20
	s_bitset1_b32 s86, 7
	v_readfirstlane_b32 s4, v0
	s_mul_i32 s3, s3, s4
	s_mul_hi_u32 s3, s4, s3
	s_add_i32 s4, s4, s3
	s_mul_hi_u32 s3, s1, s4
	s_mul_i32 s4, s3, s2
	s_sub_i32 s1, s1, s4
	s_ashr_i32 s0, s0, 31
	s_add_i32 s4, s3, 1
	s_sub_i32 s5, s1, s2
	s_cmp_ge_u32 s1, s2
	s_cselect_b32 s3, s4, s3
	s_cselect_b32 s1, s5, s1
	s_add_i32 s4, s3, 1
	s_cmp_ge_u32 s1, s2
	s_cselect_b32 s1, s4, s3
	s_xor_b32 s1, s1, s0
	s_sub_i32 s87, s1, s0
	s_mov_b32 s9, 0
	s_mov_b64 s[12:13], 0x2000000
	s_add_i32 s88, s87, -1
	v_mov_b32_e32 v161, 0
	s_movk_i32 s89, 0x104
	s_movk_i32 s90, 0x4000
	s_mov_b32 s91, 0x8000
	s_mov_b32 s92, 0xc000
	s_mov_b32 s93, 0x10000
	s_mov_b64 s[52:53], 0x80
	s_mov_b64 s[54:55], 0x32000080
	s_mov_b32 s56, 0x3e6d3388
	s_mov_b32 s58, 0x3f07dc22
	s_mov_b32 s60, 0xbf3a00e3
	s_mov_b32 s62, 0x3f35f0e3
	s_mov_b32 s64, 0xbe11a98e
	s_mov_b32 s66, 0x3e027906
	s_mov_b32 s68, 0xbf38aa3b
	s_movk_i32 s94, 0x1800
	s_mov_b32 s95, 0x2001000
	v_mov_b32_e32 v176, 1
	s_mov_b32 s96, 0
	s_branch .LBB0_218

.LBB0_228:
	v_add_u32_e32 v22, s2, v26
	v_ashrrev_i32_e32 v23, 4, v22
	v_ashrrev_i32_e32 v27, 3, v22
	v_add_u32_e32 v28, 64, v22
	v_add_u32_e32 v29, 0x80, v22
	v_add_u32_e32 v22, 0xc0, v22
	v_and_b32_e32 v30, 7, v23
	v_ashrrev_i32_e32 v32, 4, v28
	v_ashrrev_i32_e32 v33, 3, v28
	v_ashrrev_i32_e32 v28, 4, v29
	v_ashrrev_i32_e32 v36, 3, v29
	v_ashrrev_i32_e32 v29, 4, v22
	v_mad_u64_u32 v[24:25], s[6:7], v23, s89, v[18:19]
	v_and_or_b32 v40, v27, -16, v30
	v_mad_u64_u32 v[30:31], s[6:7], v32, s89, v[18:19]
	v_and_b32_e32 v27, 7, v32
	v_mad_u64_u32 v[34:35], s[6:7], v28, s89, v[18:19]
	v_and_b32_e32 v32, 7, v28
	v_mad_u64_u32 v[38:39], s[6:7], v29, s89, v[18:19]
	v_ashrrev_i32_e32 v43, 3, v22
	ds_read2_b32 v[22:23], v24 offset1:1
	ds_read2_b32 v[24:25], v24 offset0:2 offset1:3
	v_and_b32_e32 v45, 7, v29
	ds_read2_b32 v[28:29], v30 offset1:1
	ds_read2_b32 v[30:31], v30 offset0:2 offset1:3
	v_and_or_b32 v42, v33, -16, v27
	v_and_or_b32 v44, v36, -16, v32
	ds_read2_b32 v[32:33], v34 offset1:1
	ds_read2_b32 v[34:35], v34 offset0:2 offset1:3
	ds_read2_b32 v[36:37], v38 offset1:1
	ds_read2_b32 v[38:39], v38 offset0:2 offset1:3
	v_ashrrev_i32_e32 v41, 31, v40
	v_and_or_b32 v46, v43, -16, v45
	s_addk_i32 s2, 0x100
	v_lshlrev_b64 v[40:41], 11, v[40:41]
	v_ashrrev_i32_e32 v43, 31, v42
	v_ashrrev_i32_e32 v45, 31, v44
	v_ashrrev_i32_e32 v47, 31, v46
	s_cmpk_lg_i32 s2, 0x200
	v_lshl_add_u64 v[40:41], v[0:1], 0, v[40:41]
	v_lshlrev_b64 v[42:43], 11, v[42:43]
	v_lshlrev_b64 v[44:45], 11, v[44:45]
	v_lshlrev_b64 v[46:47], 11, v[46:47]
	v_lshl_add_u64 v[42:43], v[0:1], 0, v[42:43]
	v_lshl_add_u64 v[44:45], v[0:1], 0, v[44:45]
	v_lshl_add_u64 v[46:47], v[0:1], 0, v[46:47]
	s_waitcnt lgkmcnt(6)
	global_store_dwordx4 v[40:41], v[22:25], off
	s_waitcnt lgkmcnt(4)
	global_store_dwordx4 v[42:43], v[28:31], off
	s_waitcnt lgkmcnt(2)
	global_store_dwordx4 v[44:45], v[32:35], off
	s_waitcnt lgkmcnt(0)
	global_store_dwordx4 v[46:47], v[36:39], off
	s_cbranch_scc1 .LBB0_228
	s_waitcnt lgkmcnt(0)
	s_add_i32 s4, s4, s41
	s_movk_i32 s32, 0x4c00
	s_cmpk_eq_i32 s99, 0x100
	s_cselect_b32 s32, 0x3000, s32
	s_cmp_lt_i32 s4, s32
	s_cbranch_scc1 .LBB0_227

.LBB0_729:
	s_ashr_i32 s26, s52, 12
	s_add_i32 s46, s26, 28
	s_ashr_i32 s47, s46, 31
	s_lshl_b64 s[26:27], s[46:47], 25
	s_add_u32 s26, s30, s26
	s_addc_u32 s27, s31, s27
	s_lshr_b32 s40, s52, 1
	s_and_b32 s40, s40, 0x7c0
	v_add_lshl_u32 v32, s40, v76, 12
	s_and_b32 s48, s53, 0xfe0
	v_or3_b32 v82, v32, v160, s48
	v_lshl_add_u64 v[56:57], v[82:83], 2, s[26:27]
	s_cmpk_lg_i32 s99, 0x100
	s_cbranch_scc1 .Lp5dbl_noissue
	s_sub_u32 vcc_lo, s26, 0x20000000
	s_subb_u32 vcc_hi, s27, 0
	v_lshlrev_b32_e32 v226, 2, v82
	v_add_u32_e32 v230, s64, v226
	v_add_u32_e32 v234, s65, v226
	v_add_u32_e32 v238, s66, v226
	v_add_u32_e32 v242, s67, v226
	v_add_u32_e32 v246, s68, v226
	v_add_u32_e32 v250, s69, v226
	v_add_u32_e32 v178, s70, v226
	global_load_dwordx4 v[226:229], v226, vcc nt
	global_load_dwordx4 v[230:233], v230, vcc nt
	global_load_dwordx4 v[234:237], v234, vcc nt
	global_load_dwordx4 v[238:241], v238, vcc nt
	global_load_dwordx4 v[242:245], v242, vcc nt
	global_load_dwordx4 v[246:249], v246, vcc nt
	global_load_dwordx4 v[250:253], v250, vcc nt
	global_load_dwordx4 v[178:181], v178, vcc nt
.Lp5dbl_noissue:
	v_add_co_u32_e32 v36, vcc, s64, v56
	s_and_b32 s48, s77, 1
	s_nop 0
	v_addc_co_u32_e32 v37, vcc, 0, v57, vcc
	v_add_co_u32_e32 v40, vcc, s65, v56
	v_lshl_add_u32 v50, s48, 9, v161
	s_waitcnt lgkmcnt(0)
	v_addc_co_u32_e32 v41, vcc, 0, v57, vcc
	v_add_co_u32_e32 v44, vcc, s66, v56
	v_add_u32_e32 v64, 0x8000, v50
	s_nop 0
	v_addc_co_u32_e32 v45, vcc, 0, v57, vcc
	v_add_co_u32_e32 v48, vcc, s67, v56
	global_load_dwordx4 v[32:35], v[56:57], off nt
	s_nop 0
	global_load_dwordx4 v[36:39], v[36:37], off nt
	v_addc_co_u32_e32 v49, vcc, 0, v57, vcc
	global_load_dwordx4 v[40:43], v[40:41], off nt
	s_nop 0
	global_load_dwordx4 v[44:47], v[44:45], off nt
	ds_read2_b32 v[58:59], v64 offset1:16
	v_add_co_u32_e32 v52, vcc, s68, v56
	v_add_u32_e32 v152, s51, v183
	s_nop 0
	v_addc_co_u32_e32 v53, vcc, 0, v57, vcc
	global_load_dwordx4 v[48:51], v[48:49], off nt
	s_nop 0
	global_load_dwordx4 v[52:55], v[52:53], off nt
	ds_read2_b32 v[60:61], v64 offset0:32 offset1:48
	ds_read2_b32 v[62:63], v64 offset0:64 offset1:80
	s_waitcnt lgkmcnt(2)
	v_add_f32_e32 v58, 0, v58
	v_add_f32_e32 v65, v58, v59
	ds_read2_b32 v[58:59], v64 offset0:96 offset1:112
	s_waitcnt lgkmcnt(2)
	v_add_f32_e32 v60, v65, v60
	v_add_f32_e32 v60, v60, v61
	s_waitcnt lgkmcnt(1)
	v_add_f32_e32 v60, v60, v62
	v_add_f32_e32 v60, v60, v63
	s_waitcnt lgkmcnt(0)
	v_add_f32_e32 v58, v60, v58
	v_add_f32_e32 v58, v58, v59
	v_fmamk_f32 v58, v58, 0x3a000000, v184
	v_mul_f32_e32 v59, 0x4f800000, v58
	v_cmp_gt_f32_e32 vcc, s71, v58
	v_ashrrev_i32_e32 v153, 31, v152
	s_lshl_b32 s49, s48, 14
	v_cndmask_b32_e32 v60, v58, v59, vcc
	v_sqrt_f32_e32 v61, v60
	v_add_co_u32_e64 v58, s[26:27], s69, v56
	s_cmpk_eq_i32 s51, 0x70
	v_add_u32_e32 v62, -1, v61
	v_addc_co_u32_e64 v59, s[26:27], 0, v57, s[26:27]
	v_fma_f32 v63, -v62, v61, v60
	v_cmp_ge_f32_e64 s[26:27], 0, v63
	v_add_u32_e32 v63, 1, v61
	s_nop 0
	v_cndmask_b32_e64 v62, v61, v62, s[26:27]
	v_fma_f32 v61, -v63, v61, v60
	v_cmp_lt_f32_e64 s[26:27], 0, v61
	s_nop 1
	v_cndmask_b32_e64 v61, v62, v63, s[26:27]
	v_mul_f32_e32 v62, 0x37800000, v61
	v_cndmask_b32_e32 v61, v61, v62, vcc
	v_cmp_class_f32_e32 vcc, v60, v185
	s_nop 1
	v_cndmask_b32_e32 v64, v61, v60, vcc
	v_div_scale_f32 v65, s[26:27], v64, v64, 1.0
	v_rcp_f32_e32 v66, v65
	v_add_co_u32_e32 v60, vcc, s70, v56
	v_fma_f32 v67, -v65, v66, 1.0
	s_nop 0
	v_addc_co_u32_e32 v61, vcc, 0, v57, vcc
	v_fmac_f32_e32 v66, v67, v66
	v_div_scale_f32 v67, vcc, 1.0, v64, 1.0
	v_mul_f32_e32 v68, v67, v66
	v_fma_f32 v69, -v65, v68, v67
	v_fmac_f32_e32 v68, v69, v66
	v_fma_f32 v65, -v65, v68, v67
	v_div_fmas_f32 v65, v65, v66, v68
	v_div_fixup_f32 v82, v65, v64, 1.0
	v_lshlrev_b64 v[64:65], 11, v[152:153]
	global_load_dwordx4 v[56:59], v[58:59], off nt
	s_nop 0
	global_load_dwordx4 v[60:63], v[60:61], off nt
	v_lshl_add_u64 v[154:155], v[78:79], 0, v[64:65]
	ds_read_b128 v[64:67], v165
	ds_read_b128 v[68:71], v165 offset:16
	ds_read_b128 v[190:193], v165 offset:32
	ds_read_b128 v[194:197], v165 offset:48
	ds_read_b128 v[198:201], v166
	ds_read_b128 v[202:205], v166 offset:16
	ds_read_b128 v[206:209], v166 offset:32
	ds_read_b128 v[210:213], v166 offset:48
	v_pk_mul_f32 v[94:95], v[94:95], v[82:83] op_sel_hi:[1,0]
	v_pk_mul_f32 v[88:89], v[88:89], v[82:83] op_sel_hi:[1,0]
	s_waitcnt lgkmcnt(3)
	v_pk_fma_f32 v[94:95], v[66:67], v[94:95], v[200:201]
	v_pk_mul_f32 v[66:67], v[90:91], v[82:83] op_sel_hi:[1,0]
	v_pk_fma_f32 v[88:89], v[64:65], v[88:89], v[198:199]
	s_waitcnt lgkmcnt(2)
	v_pk_fma_f32 v[90:91], v[68:69], v[66:67], v[202:203]
	v_pk_mul_f32 v[68:69], v[96:97], v[82:83] op_sel_hi:[1,0]
	v_pk_mul_f32 v[66:67], v[92:93], v[82:83] op_sel_hi:[1,0]
	s_waitcnt lgkmcnt(1)
	v_pk_fma_f32 v[96:97], v[68:69], v[190:191], v[206:207]
	v_pk_mul_f32 v[68:69], v[98:99], v[82:83] op_sel_hi:[1,0]
	v_pk_fma_f32 v[92:93], v[70:71], v[66:67], v[204:205]
	v_pk_mul_f32 v[66:67], v[102:103], v[82:83] op_sel_hi:[1,0]
	s_waitcnt lgkmcnt(0)
	v_pk_fma_f32 v[98:99], v[68:69], v[194:195], v[210:211]
	v_pk_mul_f32 v[68:69], v[100:101], v[82:83] op_sel_hi:[1,0]
	v_pk_fma_f32 v[102:103], v[66:67], v[192:193], v[208:209]
	v_pk_fma_f32 v[100:101], v[68:69], v[196:197], v[212:213]
	ds_read_b128 v[68:71], v167
	ds_read_b128 v[190:193], v167 offset:16
	ds_read_b128 v[194:197], v167 offset:32
	ds_read_b128 v[198:201], v167 offset:48
	ds_read_b128 v[202:205], v168
	ds_read_b128 v[206:209], v168 offset:16
	ds_read_b128 v[210:213], v168 offset:32
	ds_read_b128 v[214:217], v168 offset:48
	v_pk_mul_f32 v[110:111], v[110:111], v[82:83] op_sel_hi:[1,0]
	v_pk_mul_f32 v[104:105], v[104:105], v[82:83] op_sel_hi:[1,0]
	s_waitcnt lgkmcnt(3)
	v_pk_fma_f32 v[110:111], v[110:111], v[70:71], v[204:205]
	v_pk_mul_f32 v[70:71], v[106:107], v[82:83] op_sel_hi:[1,0]
	v_pk_mul_f32 v[112:113], v[112:113], v[82:83] op_sel_hi:[1,0]
	s_waitcnt lgkmcnt(2)
	v_pk_fma_f32 v[106:107], v[70:71], v[190:191], v[206:207]
	v_pk_mul_f32 v[70:71], v[108:109], v[82:83] op_sel_hi:[1,0]
	v_pk_mul_f32 v[114:115], v[114:115], v[82:83] op_sel_hi:[1,0]
	v_pk_fma_f32 v[108:109], v[70:71], v[192:193], v[208:209]
	v_pk_mul_f32 v[70:71], v[118:119], v[82:83] op_sel_hi:[1,0]
	v_pk_mul_f32 v[116:117], v[116:117], v[82:83] op_sel_hi:[1,0]
	v_pk_fma_f32 v[104:105], v[104:105], v[68:69], v[202:203]
	s_waitcnt lgkmcnt(1)
	v_pk_fma_f32 v[112:113], v[112:113], v[194:195], v[210:211]
	v_pk_fma_f32 v[118:119], v[70:71], v[196:197], v[212:213]
	s_waitcnt lgkmcnt(0)
	v_pk_fma_f32 v[114:115], v[114:115], v[198:199], v[214:215]
	v_pk_fma_f32 v[116:117], v[116:117], v[200:201], v[216:217]
	ds_read_b128 v[190:193], v169
	ds_read_b128 v[194:197], v169 offset:16
	ds_read_b128 v[198:201], v169 offset:32
	ds_read_b128 v[202:205], v169 offset:48
	ds_read_b128 v[206:209], v170
	ds_read_b128 v[210:213], v170 offset:16
	ds_read_b128 v[214:217], v170 offset:32
	ds_read_b128 v[218:221], v170 offset:48
	v_pk_mul_f32 v[126:127], v[126:127], v[82:83] op_sel_hi:[1,0]
	v_pk_mul_f32 v[120:121], v[120:121], v[82:83] op_sel_hi:[1,0]
	v_pk_mul_f32 v[122:123], v[122:123], v[82:83] op_sel_hi:[1,0]
	v_pk_mul_f32 v[124:125], v[124:125], v[82:83] op_sel_hi:[1,0]
	v_pk_mul_f32 v[134:135], v[134:135], v[82:83] op_sel_hi:[1,0]
	v_pk_mul_f32 v[128:129], v[128:129], v[82:83] op_sel_hi:[1,0]
	v_pk_mul_f32 v[130:131], v[130:131], v[82:83] op_sel_hi:[1,0]
	v_pk_mul_f32 v[132:133], v[132:133], v[82:83] op_sel_hi:[1,0]
	s_waitcnt lgkmcnt(3)
	v_pk_fma_f32 v[120:121], v[120:121], v[190:191], v[206:207]
	v_pk_fma_f32 v[126:127], v[126:127], v[192:193], v[208:209]
	s_waitcnt lgkmcnt(2)
	v_pk_fma_f32 v[122:123], v[122:123], v[194:195], v[210:211]
	v_pk_fma_f32 v[124:125], v[124:125], v[196:197], v[212:213]
	s_waitcnt lgkmcnt(1)
	v_pk_fma_f32 v[128:129], v[128:129], v[198:199], v[214:215]
	v_pk_fma_f32 v[134:135], v[134:135], v[200:201], v[216:217]
	s_waitcnt lgkmcnt(0)
	v_pk_fma_f32 v[130:131], v[130:131], v[202:203], v[218:219]
	v_pk_fma_f32 v[132:133], v[132:133], v[204:205], v[220:221]
	ds_read_b128 v[194:197], v171
	ds_read_b128 v[198:201], v171 offset:16
	ds_read_b128 v[202:205], v171 offset:32
	ds_read_b128 v[206:209], v171 offset:48
	ds_read_b128 v[210:213], v172
	ds_read_b128 v[214:217], v172 offset:16
	ds_read_b128 v[218:221], v172 offset:32
	ds_read_b128 v[222:225], v172 offset:48
	v_mov_b32_e32 v64, v83
	v_mov_b32_e32 v65, v83
	v_mov_b32_e32 v66, v83
	v_mov_b32_e32 v67, v83
	v_cvt_pk_fp8_f32 v64, v88, v89
	v_cvt_pk_fp8_f32 v65, v90, v91
	v_cvt_pk_fp8_f32 v66, v96, v97
	v_cvt_pk_fp8_f32 v67, v98, v99
	v_mov_b32_e32 v68, v83
	v_mov_b32_e32 v69, v83
	v_mov_b32_e32 v70, v83
	v_mov_b32_e32 v71, v83
	v_cvt_pk_fp8_f32 v68, v104, v105
	v_cvt_pk_fp8_f32 v69, v106, v107
	v_cvt_pk_fp8_f32 v70, v112, v113
	v_cvt_pk_fp8_f32 v71, v114, v115
	v_mov_b32_e32 v190, v83
	v_mov_b32_e32 v191, v83
	v_mov_b32_e32 v192, v83
	v_mov_b32_e32 v193, v83
	v_pk_mul_f32 v[142:143], v[142:143], v[82:83] op_sel_hi:[1,0]
	v_pk_mul_f32 v[136:137], v[136:137], v[82:83] op_sel_hi:[1,0]
	v_pk_mul_f32 v[138:139], v[138:139], v[82:83] op_sel_hi:[1,0]
	v_pk_mul_f32 v[144:145], v[144:145], v[82:83] op_sel_hi:[1,0]
	v_pk_mul_f32 v[146:147], v[146:147], v[82:83] op_sel_hi:[1,0]
	v_cvt_pk_fp8_f32 v190, v120, v121
	v_cvt_pk_fp8_f32 v191, v122, v123
	v_cvt_pk_fp8_f32 v192, v128, v129
	v_cvt_pk_fp8_f32 v193, v130, v131
	s_waitcnt lgkmcnt(3)
	v_pk_fma_f32 v[136:137], v[136:137], v[194:195], v[210:211]
	v_pk_fma_f32 v[142:143], v[142:143], v[196:197], v[212:213]
	v_mov_b32_e32 v194, v83
	s_waitcnt lgkmcnt(2)
	v_pk_fma_f32 v[138:139], v[138:139], v[198:199], v[214:215]
	v_mov_b32_e32 v195, v83
	s_waitcnt lgkmcnt(1)
	v_pk_fma_f32 v[144:145], v[144:145], v[202:203], v[218:219]
	v_mov_b32_e32 v196, v83
	s_waitcnt lgkmcnt(0)
	v_pk_fma_f32 v[146:147], v[146:147], v[206:207], v[222:223]
	v_mov_b32_e32 v197, v83
	v_cvt_pk_fp8_f32 v194, v136, v137
	v_cvt_pk_fp8_f32 v195, v138, v139
	v_cvt_pk_fp8_f32 v196, v144, v145
	v_cvt_pk_fp8_f32 v197, v146, v147
	v_cvt_pk_fp8_f32 v64, v94, v95 op_sel:[0,0,1]
	v_cvt_pk_fp8_f32 v65, v92, v93 op_sel:[0,0,1]
	v_cvt_pk_fp8_f32 v66, v102, v103 op_sel:[0,0,1]
	v_cvt_pk_fp8_f32 v67, v100, v101 op_sel:[0,0,1]
	v_cvt_pk_fp8_f32 v68, v110, v111 op_sel:[0,0,1]
	v_cvt_pk_fp8_f32 v69, v108, v109 op_sel:[0,0,1]
	v_cvt_pk_fp8_f32 v70, v118, v119 op_sel:[0,0,1]
	v_cvt_pk_fp8_f32 v71, v116, v117 op_sel:[0,0,1]
	v_pk_mul_f32 v[140:141], v[140:141], v[82:83] op_sel_hi:[1,0]
	v_pk_mul_f32 v[150:151], v[150:151], v[82:83] op_sel_hi:[1,0]
	v_pk_mul_f32 v[148:149], v[148:149], v[82:83] op_sel_hi:[1,0]
	v_cvt_pk_fp8_f32 v190, v126, v127 op_sel:[0,0,1]
	v_cvt_pk_fp8_f32 v191, v124, v125 op_sel:[0,0,1]
	v_cvt_pk_fp8_f32 v192, v134, v135 op_sel:[0,0,1]
	v_cvt_pk_fp8_f32 v193, v132, v133 op_sel:[0,0,1]
	v_pk_fma_f32 v[140:141], v[140:141], v[200:201], v[216:217]
	v_pk_fma_f32 v[150:151], v[150:151], v[204:205], v[220:221]
	v_pk_fma_f32 v[148:149], v[148:149], v[208:209], v[224:225]
	v_cvt_pk_fp8_f32 v194, v142, v143 op_sel:[0,0,1]
	v_cvt_pk_fp8_f32 v195, v140, v141 op_sel:[0,0,1]
	v_cvt_pk_fp8_f32 v196, v150, v151 op_sel:[0,0,1]
	v_cvt_pk_fp8_f32 v197, v148, v149 op_sel:[0,0,1]
	global_store_dwordx4 v[154:155], v[64:67], off
	global_store_dwordx4 v[154:155], v[68:71], off offset:64
	global_store_dwordx4 v[154:155], v[190:193], off offset:128
	global_store_dwordx4 v[154:155], v[194:197], off offset:192
	v_mov_b32_e32 v64, v162
	v_add_u32_e32 v82, s49, v177
	v_ashrrev_i32_e32 v65, 31, v64
	v_lshl_add_u64 v[64:65], v[64:65], 2, s[34:35]
	v_add_co_u32_e32 v70, vcc, s62, v64
	global_load_dwordx4 v[66:69], v[64:65], off
	global_load_dwordx4 v[190:193], v[64:65], off offset:1024
	v_addc_co_u32_e32 v71, vcc, 0, v65, vcc
	global_load_dwordx4 v[198:201], v[70:71], off offset:-4096
	v_add_co_u32_e32 v154, vcc, s75, v64
	s_waitcnt vmcnt(2)
	v_mfma_f32_16x16x4_f32 v[194:197], v88, v66, 0
	v_addc_co_u32_e32 v155, vcc, 0, v65, vcc
	global_load_dwordx4 v[202:205], v[154:155], off offset:3072
	v_add_co_u32_e32 v210, vcc, s72, v64
	s_nop 1
	v_addc_co_u32_e32 v211, vcc, 0, v65, vcc
	s_waitcnt vmcnt(1)
	v_mfma_f32_16x16x4_f32 v[206:209], v88, v198, 0
	v_add_co_u32_e32 v218, vcc, s61, v64
	s_nop 1
	v_addc_co_u32_e32 v219, vcc, 0, v65, vcc
	v_add_co_u32_e32 v220, vcc, s64, v64
	v_mfma_f32_16x16x4_f32 v[194:197], v89, v67, v[194:197]
	s_nop 0
	v_addc_co_u32_e32 v221, vcc, 0, v65, vcc
	v_mfma_f32_16x16x4_f32 v[206:209], v89, v199, v[206:209]
	v_mfma_f32_16x16x4_f32 v[194:197], v94, v68, v[194:197]
	v_mfma_f32_16x16x4_f32 v[206:209], v94, v200, v[206:209]
	v_mfma_f32_16x16x4_f32 v[66:69], v95, v69, v[194:197]
	v_mfma_f32_16x16x4_f32 v[194:197], v95, v201, v[206:209]
	global_load_dwordx4 v[198:201], v[210:211], off offset:1024
	s_nop 6
	global_load_dwordx4 v[206:209], v[210:211], off offset:2048
	v_mfma_f32_16x16x4_f32 v[66:69], v90, v190, v[66:69]
	v_mfma_f32_16x16x4_f32 v[66:69], v91, v191, v[66:69]
	v_mfma_f32_16x16x4_f32 v[66:69], v92, v192, v[66:69]
	v_mfma_f32_16x16x4_f32 v[66:69], v93, v193, v[66:69]
	global_load_dwordx4 v[190:193], v[64:65], off offset:2048
	s_waitcnt vmcnt(2)
	v_mfma_f32_16x16x4_f32 v[194:197], v90, v198, v[194:197]
	v_mfma_f32_16x16x4_f32 v[194:197], v91, v199, v[194:197]
	v_mfma_f32_16x16x4_f32 v[194:197], v92, v200, v[194:197]
	v_mfma_f32_16x16x4_f32 v[194:197], v93, v201, v[194:197]
	global_load_dwordx4 v[198:201], v[64:65], off offset:3072
	s_waitcnt vmcnt(1)
	v_mfma_f32_16x16x4_f32 v[66:69], v96, v190, v[66:69]
	v_mfma_f32_16x16x4_f32 v[194:197], v96, v206, v[194:197]
	v_mfma_f32_16x16x4_f32 v[66:69], v97, v191, v[66:69]
	v_mfma_f32_16x16x4_f32 v[194:197], v97, v207, v[194:197]
	v_mfma_f32_16x16x4_f32 v[66:69], v102, v192, v[66:69]
	v_mfma_f32_16x16x4_f32 v[194:197], v102, v208, v[194:197]
	v_mfma_f32_16x16x4_f32 v[66:69], v103, v193, v[66:69]
	v_mfma_f32_16x16x4_f32 v[190:193], v103, v209, v[194:197]
	s_nop 7
	global_load_dwordx4 v[194:197], v[210:211], off offset:3072
	global_load_dwordx4 v[206:209], v[218:219], off offset:1024
	s_waitcnt vmcnt(1)
	v_mfma_f32_16x16x4_f32 v[190:193], v98, v194, v[190:193]
	v_mfma_f32_16x16x4_f32 v[190:193], v99, v195, v[190:193]
	v_mfma_f32_16x16x4_f32 v[190:193], v100, v196, v[190:193]
	v_mfma_f32_16x16x4_f32 v[190:193], v101, v197, v[190:193]
	global_load_dwordx4 v[194:197], v[70:71], off
	v_mfma_f32_16x16x4_f32 v[66:69], v98, v198, v[66:69]
	v_mfma_f32_16x16x4_f32 v[66:69], v99, v199, v[66:69]
	v_mfma_f32_16x16x4_f32 v[66:69], v100, v200, v[66:69]
	v_mfma_f32_16x16x4_f32 v[66:69], v101, v201, v[66:69]
	global_load_dwordx4 v[198:201], v[70:71], off offset:1024
	global_load_dwordx4 v[210:213], v[220:221], off offset:-4096
	global_load_dwordx4 v[214:217], v[220:221], off
	s_waitcnt vmcnt(3)
	v_mfma_f32_16x16x4_f32 v[66:69], v104, v194, v[66:69]
	v_mfma_f32_16x16x4_f32 v[66:69], v105, v195, v[66:69]
	v_mfma_f32_16x16x4_f32 v[66:69], v110, v196, v[66:69]
	v_mfma_f32_16x16x4_f32 v[66:69], v111, v197, v[66:69]
	global_load_dwordx4 v[194:197], v[70:71], off offset:2048
	s_waitcnt vmcnt(3)
	v_mfma_f32_16x16x4_f32 v[66:69], v106, v198, v[66:69]
	v_mfma_f32_16x16x4_f32 v[66:69], v107, v199, v[66:69]
	v_mfma_f32_16x16x4_f32 v[66:69], v108, v200, v[66:69]
	v_mfma_f32_16x16x4_f32 v[66:69], v109, v201, v[66:69]
	global_load_dwordx4 v[198:201], v[218:219], off offset:2048
	s_waitcnt vmcnt(3)
	v_mfma_f32_16x16x4_f32 v[190:193], v104, v210, v[190:193]
	v_mfma_f32_16x16x4_f32 v[190:193], v105, v211, v[190:193]
	v_mfma_f32_16x16x4_f32 v[190:193], v110, v212, v[190:193]
	v_mfma_f32_16x16x4_f32 v[190:193], v111, v213, v[190:193]
	global_load_dwordx4 v[210:213], v[218:219], off offset:3072
	v_add_co_u32_e32 v218, vcc, s74, v64
	s_nop 1
	v_addc_co_u32_e32 v219, vcc, 0, v65, vcc
	v_mfma_f32_16x16x4_f32 v[190:193], v106, v206, v[190:193]
	v_mfma_f32_16x16x4_f32 v[190:193], v107, v207, v[190:193]
	v_mfma_f32_16x16x4_f32 v[190:193], v108, v208, v[190:193]
	v_mfma_f32_16x16x4_f32 v[190:193], v109, v209, v[190:193]
	global_load_dwordx4 v[206:209], v[70:71], off offset:3072
	s_waitcnt vmcnt(3)
	v_mfma_f32_16x16x4_f32 v[66:69], v112, v194, v[66:69]
	s_waitcnt vmcnt(2)
	v_mfma_f32_16x16x4_f32 v[190:193], v112, v198, v[190:193]
	v_mfma_f32_16x16x4_f32 v[66:69], v113, v195, v[66:69]
	v_mfma_f32_16x16x4_f32 v[190:193], v113, v199, v[190:193]
	v_mfma_f32_16x16x4_f32 v[66:69], v118, v196, v[66:69]
	v_mfma_f32_16x16x4_f32 v[190:193], v118, v200, v[190:193]
	v_mfma_f32_16x16x4_f32 v[66:69], v119, v197, v[66:69]
	v_mfma_f32_16x16x4_f32 v[190:193], v119, v201, v[190:193]
	global_load_dwordx4 v[194:197], v[218:219], off offset:-4096
	global_load_dwordx4 v[198:201], v[220:221], off offset:3072
	s_waitcnt vmcnt(2)
	v_mfma_f32_16x16x4_f32 v[66:69], v114, v206, v[66:69]
	v_mfma_f32_16x16x4_f32 v[190:193], v114, v210, v[190:193]
	v_mfma_f32_16x16x4_f32 v[66:69], v115, v207, v[66:69]
	v_mfma_f32_16x16x4_f32 v[190:193], v115, v211, v[190:193]
	v_mfma_f32_16x16x4_f32 v[66:69], v116, v208, v[66:69]
	v_mfma_f32_16x16x4_f32 v[190:193], v116, v212, v[190:193]
	v_mfma_f32_16x16x4_f32 v[66:69], v117, v209, v[66:69]
	global_load_dwordx4 v[206:209], v[220:221], off offset:1024
	v_mfma_f32_16x16x4_f32 v[190:193], v117, v213, v[190:193]
	v_mfma_f32_16x16x4_f32 v[66:69], v120, v214, v[66:69]
	v_add_co_u32_e32 v214, vcc, s73, v64
	s_waitcnt vmcnt(2)
	v_mfma_f32_16x16x4_f32 v[190:193], v120, v194, v[190:193]
	v_mfma_f32_16x16x4_f32 v[66:69], v121, v215, v[66:69]
	v_addc_co_u32_e32 v215, vcc, 0, v65, vcc
	global_load_dwordx4 v[210:213], v[214:215], off offset:2048
	v_mfma_f32_16x16x4_f32 v[190:193], v121, v195, v[190:193]
	v_mfma_f32_16x16x4_f32 v[66:69], v126, v216, v[66:69]
	v_mfma_f32_16x16x4_f32 v[190:193], v126, v196, v[190:193]
	v_mfma_f32_16x16x4_f32 v[64:67], v127, v217, v[66:69]
	s_nop 7
	global_load_dwordx4 v[68:71], v[214:215], off offset:1024
	v_mfma_f32_16x16x4_f32 v[190:193], v127, v197, v[190:193]
	global_load_dwordx4 v[194:197], v[220:221], off offset:2048
	s_waitcnt vmcnt(3)
	v_mfma_f32_16x16x4_f32 v[64:67], v122, v206, v[64:67]
	v_mfma_f32_16x16x4_f32 v[64:67], v123, v207, v[64:67]
	v_mfma_f32_16x16x4_f32 v[64:67], v124, v208, v[64:67]
	v_mfma_f32_16x16x4_f32 v[64:67], v125, v209, v[64:67]
	s_waitcnt vmcnt(1)
	v_mfma_f32_16x16x4_f32 v[190:193], v122, v68, v[190:193]
	s_waitcnt vmcnt(0)
	v_mfma_f32_16x16x4_f32 v[64:67], v128, v194, v[64:67]
	v_mfma_f32_16x16x4_f32 v[190:193], v123, v69, v[190:193]
	v_mfma_f32_16x16x4_f32 v[64:67], v129, v195, v[64:67]
	v_mfma_f32_16x16x4_f32 v[190:193], v124, v70, v[190:193]
	v_mfma_f32_16x16x4_f32 v[64:67], v134, v196, v[64:67]
	v_mfma_f32_16x16x4_f32 v[68:71], v125, v71, v[190:193]
	v_mfma_f32_16x16x4_f32 v[64:67], v135, v197, v[64:67]
	s_nop 6
	global_load_dwordx4 v[190:193], v[214:215], off offset:3072
	global_load_dwordx4 v[194:197], v[154:155], off
	v_mfma_f32_16x16x4_f32 v[64:67], v130, v198, v[64:67]
	v_mfma_f32_16x16x4_f32 v[64:67], v131, v199, v[64:67]
	v_mfma_f32_16x16x4_f32 v[64:67], v132, v200, v[64:67]
	v_mfma_f32_16x16x4_f32 v[64:67], v133, v201, v[64:67]
	global_load_dwordx4 v[198:201], v[218:219], off
	v_mfma_f32_16x16x4_f32 v[68:71], v128, v210, v[68:71]
	v_mfma_f32_16x16x4_f32 v[68:71], v129, v211, v[68:71]
	v_mfma_f32_16x16x4_f32 v[68:71], v134, v212, v[68:71]
	v_mfma_f32_16x16x4_f32 v[68:71], v135, v213, v[68:71]
	s_waitcnt vmcnt(2)
	v_mfma_f32_16x16x4_f32 v[68:71], v130, v190, v[68:71]
	v_mfma_f32_16x16x4_f32 v[68:71], v131, v191, v[68:71]
	v_mfma_f32_16x16x4_f32 v[68:71], v132, v192, v[68:71]
	v_mfma_f32_16x16x4_f32 v[68:71], v133, v193, v[68:71]
	global_load_dwordx4 v[190:193], v[218:219], off offset:1024
	s_waitcnt vmcnt(1)
	v_mfma_f32_16x16x4_f32 v[64:67], v136, v198, v[64:67]
	v_mfma_f32_16x16x4_f32 v[68:71], v136, v194, v[68:71]
	v_mfma_f32_16x16x4_f32 v[64:67], v137, v199, v[64:67]
	v_mfma_f32_16x16x4_f32 v[68:71], v137, v195, v[68:71]
	v_mfma_f32_16x16x4_f32 v[64:67], v142, v200, v[64:67]
	v_mfma_f32_16x16x4_f32 v[68:71], v142, v196, v[68:71]
	v_mfma_f32_16x16x4_f32 v[64:67], v143, v201, v[64:67]
	v_mfma_f32_16x16x4_f32 v[68:71], v143, v197, v[68:71]
	global_load_dwordx4 v[194:197], v[154:155], off offset:1024
	global_load_dwordx4 v[198:201], v[154:155], off offset:2048
	s_waitcnt vmcnt(2)
	v_mfma_f32_16x16x4_f32 v[64:67], v138, v190, v[64:67]
	v_mfma_f32_16x16x4_f32 v[64:67], v139, v191, v[64:67]
	v_mfma_f32_16x16x4_f32 v[64:67], v140, v192, v[64:67]
	v_mfma_f32_16x16x4_f32 v[64:67], v141, v193, v[64:67]
	global_load_dwordx4 v[190:193], v[218:219], off offset:2048
	s_waitcnt vmcnt(2)
	v_mfma_f32_16x16x4_f32 v[68:71], v138, v194, v[68:71]
	v_mfma_f32_16x16x4_f32 v[68:71], v139, v195, v[68:71]
	v_mfma_f32_16x16x4_f32 v[68:71], v140, v196, v[68:71]
	v_mfma_f32_16x16x4_f32 v[68:71], v141, v197, v[68:71]
	global_load_dwordx4 v[194:197], v[218:219], off offset:3072
	s_waitcnt vmcnt(1)
	v_mfma_f32_16x16x4_f32 v[64:67], v144, v190, v[64:67]
	v_mfma_f32_16x16x4_f32 v[68:71], v144, v198, v[68:71]
	v_mfma_f32_16x16x4_f32 v[64:67], v145, v191, v[64:67]
	v_mfma_f32_16x16x4_f32 v[68:71], v145, v199, v[68:71]
	v_mfma_f32_16x16x4_f32 v[64:67], v150, v192, v[64:67]
	v_mfma_f32_16x16x4_f32 v[68:71], v150, v200, v[68:71]
	v_mfma_f32_16x16x4_f32 v[64:67], v151, v193, v[64:67]
	v_mfma_f32_16x16x4_f32 v[68:71], v151, v201, v[68:71]
	s_waitcnt vmcnt(0)
	v_mfma_f32_16x16x4_f32 v[64:67], v146, v194, v[64:67]
	v_mfma_f32_16x16x4_f32 v[68:71], v146, v202, v[68:71]
	v_mfma_f32_16x16x4_f32 v[64:67], v147, v195, v[64:67]
	v_mfma_f32_16x16x4_f32 v[68:71], v147, v203, v[68:71]
	v_mfma_f32_16x16x4_f32 v[64:67], v148, v196, v[64:67]
	v_mfma_f32_16x16x4_f32 v[68:71], v148, v204, v[68:71]
	v_mfma_f32_16x16x4_f32 v[64:67], v149, v197, v[64:67]
	v_mfma_f32_16x16x4_f32 v[68:71], v149, v205, v[68:71]
	s_nop 9
	ds_write2_b32 v82, v64, v68 offset1:16
	ds_write2_b32 v82, v65, v69 offset0:32 offset1:48
	ds_write2_b32 v82, v66, v70 offset0:64 offset1:80
	ds_write2_b32 v82, v67, v71 offset0:96 offset1:112
	s_cbranch_scc1 .LBB0_734
	v_and_b32_e32 v89, 0xffff0000, v4
	v_and_b32_e32 v95, 0xffff0000, v5
	v_lshlrev_b32_e32 v88, 16, v4
	v_lshlrev_b32_e32 v94, 16, v5
	v_mul_f32_e32 v64, v89, v89
	v_mul_f32_e32 v65, v95, v95
	v_and_b32_e32 v91, 0xffff0000, v6
	v_fmac_f32_e32 v64, v88, v88
	v_fmac_f32_e32 v65, v94, v94
	v_lshlrev_b32_e32 v90, 16, v6
	v_add_f32_e32 v64, v64, v65
	v_mul_f32_e32 v65, v91, v91
	v_and_b32_e32 v93, 0xffff0000, v7
	v_fmac_f32_e32 v65, v90, v90
	v_lshlrev_b32_e32 v92, 16, v7
	v_add_f32_e32 v64, v65, v64
	v_mul_f32_e32 v65, v93, v93
	v_fmac_f32_e32 v65, v92, v92
	v_and_b32_e32 v97, 0xffff0000, v0
	v_and_b32_e32 v103, 0xffff0000, v1
	v_add_f32_e32 v64, v65, v64
	v_lshlrev_b32_e32 v96, 16, v0
	v_lshlrev_b32_e32 v102, 16, v1
	v_mul_f32_e32 v65, v97, v97
	v_mul_f32_e32 v66, v103, v103
	v_and_b32_e32 v99, 0xffff0000, v2
	v_fmac_f32_e32 v65, v96, v96
	v_fmac_f32_e32 v66, v102, v102
	v_lshlrev_b32_e32 v98, 16, v2
	v_add_f32_e32 v65, v65, v66
	v_mul_f32_e32 v66, v99, v99
	v_and_b32_e32 v101, 0xffff0000, v3
	v_fmac_f32_e32 v66, v98, v98
	v_lshlrev_b32_e32 v100, 16, v3
	v_add_f32_e32 v65, v66, v65
	v_mul_f32_e32 v66, v101, v101
	v_fmac_f32_e32 v66, v100, v100
	v_add_f32_e32 v65, v66, v65
	v_and_b32_e32 v105, 0xffff0000, v12
	v_and_b32_e32 v111, 0xffff0000, v13
	v_add_f32_e32 v64, v64, v65
	v_lshlrev_b32_e32 v104, 16, v12
	v_lshlrev_b32_e32 v110, 16, v13
	v_mul_f32_e32 v65, v105, v105
	v_mul_f32_e32 v66, v111, v111
	v_and_b32_e32 v107, 0xffff0000, v14
	v_fmac_f32_e32 v65, v104, v104
	v_fmac_f32_e32 v66, v110, v110
	v_lshlrev_b32_e32 v106, 16, v14
	v_add_f32_e32 v65, v65, v66
	v_mul_f32_e32 v66, v107, v107
	v_and_b32_e32 v109, 0xffff0000, v15
	v_fmac_f32_e32 v66, v106, v106
	v_lshlrev_b32_e32 v108, 16, v15
	v_add_f32_e32 v65, v66, v65
	v_mul_f32_e32 v66, v109, v109
	v_fmac_f32_e32 v66, v108, v108
	v_add_f32_e32 v65, v66, v65
	v_and_b32_e32 v113, 0xffff0000, v8
	v_and_b32_e32 v119, 0xffff0000, v9
	v_add_f32_e32 v64, v64, v65
	v_lshlrev_b32_e32 v112, 16, v8
	v_lshlrev_b32_e32 v118, 16, v9
	v_mul_f32_e32 v65, v113, v113
	v_mul_f32_e32 v66, v119, v119
	v_and_b32_e32 v115, 0xffff0000, v10
	v_fmac_f32_e32 v65, v112, v112
	v_fmac_f32_e32 v66, v118, v118
	v_lshlrev_b32_e32 v114, 16, v10
	v_add_f32_e32 v65, v65, v66
	v_mul_f32_e32 v66, v115, v115
	v_and_b32_e32 v117, 0xffff0000, v11
	v_fmac_f32_e32 v66, v114, v114
	v_lshlrev_b32_e32 v116, 16, v11
	v_add_f32_e32 v65, v66, v65
	v_mul_f32_e32 v66, v117, v117
	v_fmac_f32_e32 v66, v116, v116
	v_add_f32_e32 v65, v66, v65
	v_and_b32_e32 v121, 0xffff0000, v20
	v_and_b32_e32 v127, 0xffff0000, v21
	v_add_f32_e32 v64, v64, v65
	v_lshlrev_b32_e32 v120, 16, v20
	v_lshlrev_b32_e32 v126, 16, v21
	v_mul_f32_e32 v65, v121, v121
	v_mul_f32_e32 v66, v127, v127
	v_and_b32_e32 v123, 0xffff0000, v22
	v_fmac_f32_e32 v65, v120, v120
	v_fmac_f32_e32 v66, v126, v126
	v_lshlrev_b32_e32 v122, 16, v22
	v_add_f32_e32 v65, v65, v66
	v_mul_f32_e32 v66, v123, v123
	v_and_b32_e32 v125, 0xffff0000, v23
	v_fmac_f32_e32 v66, v122, v122
	v_lshlrev_b32_e32 v124, 16, v23
	v_add_f32_e32 v65, v66, v65
	v_mul_f32_e32 v66, v125, v125
	v_fmac_f32_e32 v66, v124, v124
	v_add_f32_e32 v65, v66, v65
	v_and_b32_e32 v129, 0xffff0000, v16
	v_and_b32_e32 v135, 0xffff0000, v17
	v_add_f32_e32 v64, v64, v65
	v_lshlrev_b32_e32 v128, 16, v16
	v_lshlrev_b32_e32 v134, 16, v17
	v_mul_f32_e32 v65, v129, v129
	v_mul_f32_e32 v66, v135, v135
	v_and_b32_e32 v131, 0xffff0000, v18
	v_fmac_f32_e32 v65, v128, v128
	v_fmac_f32_e32 v66, v134, v134
	v_lshlrev_b32_e32 v130, 16, v18
	v_add_f32_e32 v65, v65, v66
	v_mul_f32_e32 v66, v131, v131
	v_and_b32_e32 v133, 0xffff0000, v19
	v_fmac_f32_e32 v66, v130, v130
	v_lshlrev_b32_e32 v132, 16, v19
	v_add_f32_e32 v65, v66, v65
	v_mul_f32_e32 v66, v133, v133
	v_fmac_f32_e32 v66, v132, v132
	v_add_f32_e32 v65, v66, v65
	v_and_b32_e32 v137, 0xffff0000, v28
	v_and_b32_e32 v143, 0xffff0000, v29
	v_add_f32_e32 v64, v64, v65
	v_lshlrev_b32_e32 v136, 16, v28
	v_lshlrev_b32_e32 v142, 16, v29
	v_mul_f32_e32 v65, v137, v137
	v_mul_f32_e32 v66, v143, v143
	v_and_b32_e32 v139, 0xffff0000, v30
	v_fmac_f32_e32 v65, v136, v136
	v_fmac_f32_e32 v66, v142, v142
	v_lshlrev_b32_e32 v138, 16, v30
	v_add_f32_e32 v65, v65, v66
	v_mul_f32_e32 v66, v139, v139
	v_and_b32_e32 v141, 0xffff0000, v31
	v_fmac_f32_e32 v66, v138, v138
	v_lshlrev_b32_e32 v140, 16, v31
	v_add_f32_e32 v65, v66, v65
	v_mul_f32_e32 v66, v141, v141
	v_fmac_f32_e32 v66, v140, v140
	v_add_f32_e32 v65, v66, v65
	v_and_b32_e32 v145, 0xffff0000, v24
	v_and_b32_e32 v151, 0xffff0000, v25
	v_add_f32_e32 v64, v64, v65
	v_lshlrev_b32_e32 v144, 16, v24
	v_lshlrev_b32_e32 v150, 16, v25
	v_mul_f32_e32 v65, v145, v145
	v_mul_f32_e32 v66, v151, v151
	v_and_b32_e32 v147, 0xffff0000, v26
	v_fmac_f32_e32 v65, v144, v144
	v_fmac_f32_e32 v66, v150, v150
	v_lshlrev_b32_e32 v146, 16, v26
	v_add_f32_e32 v65, v65, v66
	v_mul_f32_e32 v66, v147, v147
	v_and_b32_e32 v149, 0xffff0000, v27
	v_fmac_f32_e32 v66, v146, v146
	v_lshlrev_b32_e32 v148, 16, v27
	v_add_f32_e32 v65, v66, v65
	v_mul_f32_e32 v66, v149, v149
	v_fmac_f32_e32 v66, v148, v148
	v_add_f32_e32 v65, v66, v65
	v_add_f32_e32 v64, v64, v65
	ds_bpermute_b32 v65, v157, v64
	s_waitcnt lgkmcnt(0)
	v_add_f32_e32 v64, v64, v65
	ds_bpermute_b32 v65, v158, v64
	s_and_saveexec_b64 s[26:27], s[6:7]
	s_cbranch_execz .LBB0_732
	s_lshl_b32 s48, s48, 9
	s_xor_b32 s48, s48, 0x200
	s_waitcnt lgkmcnt(0)
	v_add_f32_e32 v64, v64, v65
	v_add_u32_e32 v65, s48, v159
	ds_write_b32 v65, v64 offset:32768

.LBB0_734:
	v_mul_f32_e32 v32, 0x43800000, v32
	v_mul_f32_e32 v36, 0x43800000, v36
	v_mov_b32_e32 v66, v83
	v_cvt_pk_fp8_f32 v66, v32, v36
	v_mul_f32_e32 v32, 0x43800000, v48
	v_mul_f32_e32 v36, 0x43800000, v52
	v_mov_b32_e32 v67, v83
	v_cvt_pk_fp8_f32 v67, v32, v36
	v_mul_f32_e32 v32, 0x43800000, v56
	v_mul_f32_e32 v36, 0x43800000, v60
	s_lshr_b32 s26, s53, 8
	v_cvt_pk_fp8_f32 v67, v32, v36 op_sel:[0,0,1]
	v_mul_f32_e32 v33, 0x43800000, v33
	v_mul_f32_e32 v36, 0x43800000, v37
	v_mov_b32_e32 v32, v83
	s_and_b32 s26, s26, 8
	v_mul_f32_e32 v37, 0x43800000, v41
	v_cvt_pk_fp8_f32 v32, v33, v36
	v_mul_f32_e32 v36, 0x43800000, v49
	v_mul_f32_e32 v41, 0x43800000, v53
	v_mov_b32_e32 v33, v83
	s_or_b32 s48, s50, s26
	s_lshl_b64 s[26:27], s[46:47], 12
	v_cvt_pk_fp8_f32 v33, v36, v41
	s_or_b32 s26, s26, s48
	v_mul_f32_e32 v40, 0x43800000, v40
	v_mul_f32_e32 v44, 0x43800000, v44
	s_waitcnt lgkmcnt(0)
	v_mov_b32_e32 v65, s27
	v_or_b32_e32 v64, s26, v80
	v_cvt_pk_fp8_f32 v66, v40, v44 op_sel:[0,0,1]
	v_mul_f32_e32 v40, 0x43800000, v45
	v_lshlrev_b64 v[64:65], 11, v[64:65]
	v_cvt_pk_fp8_f32 v32, v37, v40 op_sel:[0,0,1]
	v_mul_f32_e32 v36, 0x43800000, v57
	v_mul_f32_e32 v37, 0x43800000, v61
	v_lshl_add_u64 v[64:65], s[28:29], 0, v[64:65]
	v_cvt_pk_fp8_f32 v33, v36, v37 op_sel:[0,0,1]
	v_lshl_add_u64 v[36:37], v[64:65], 0, s[40:41]
	v_lshl_add_u64 v[36:37], v[36:37], 0, v[76:77]
	global_store_dwordx2 v[36:37], v[66:67], off
	global_store_dwordx2 v[36:37], v[32:33], off offset:2048
	v_mul_f32_e32 v33, 0x43800000, v34
	v_mul_f32_e32 v34, 0x43800000, v38
	v_mov_b32_e32 v32, v83
	v_cvt_pk_fp8_f32 v32, v33, v34
	v_mul_f32_e32 v34, 0x43800000, v50
	v_mul_f32_e32 v41, 0x43800000, v54
	v_mov_b32_e32 v33, v83
	v_cvt_pk_fp8_f32 v33, v34, v41
	v_mul_f32_e32 v38, 0x43800000, v42
	v_mul_f32_e32 v40, 0x43800000, v46
	v_cvt_pk_fp8_f32 v32, v38, v40 op_sel:[0,0,1]
	v_mul_f32_e32 v34, 0x43800000, v58
	v_mul_f32_e32 v38, 0x43800000, v62
	v_cvt_pk_fp8_f32 v33, v34, v38 op_sel:[0,0,1]
	v_mul_f32_e32 v35, 0x43800000, v35
	v_mul_f32_e32 v38, 0x43800000, v39
	v_mov_b32_e32 v34, v83
	v_cvt_pk_fp8_f32 v34, v35, v38
	v_mul_f32_e32 v38, 0x43800000, v51
	v_mul_f32_e32 v41, 0x43800000, v55
	v_mov_b32_e32 v35, v83
	v_cvt_pk_fp8_f32 v35, v38, v41
	v_mul_f32_e32 v39, 0x43800000, v43
	v_mul_f32_e32 v40, 0x43800000, v47
	v_cvt_pk_fp8_f32 v34, v39, v40 op_sel:[0,0,1]
	v_mul_f32_e32 v38, 0x43800000, v59
	v_mul_f32_e32 v39, 0x43800000, v63
	v_cvt_pk_fp8_f32 v35, v38, v39 op_sel:[0,0,1]
	v_add_co_u32_e32 v36, vcc, s72, v36
	v_add_u32_e32 v38, s49, v164
	s_nop 0
	v_addc_co_u32_e32 v37, vcc, 0, v37, vcc
	global_store_dwordx2 v[36:37], v[32:33], off
	global_store_dwordx2 v[36:37], v[34:35], off offset:2048
	s_cmpk_lg_i32 s99, 0x100
	s_cbranch_scc1 .Lp5dbl_noconsume
	s_sub_i32 s46, s46, 16
	v_mul_f32_e32 v226, 0x43800000, v226
	v_mul_f32_e32 v230, 0x43800000, v230
	v_mov_b32_e32 v66, v83
	v_cvt_pk_fp8_f32 v66, v226, v230
	v_mul_f32_e32 v226, 0x43800000, v242
	v_mul_f32_e32 v230, 0x43800000, v246
	v_mov_b32_e32 v67, v83
	v_cvt_pk_fp8_f32 v67, v226, v230
	v_mul_f32_e32 v226, 0x43800000, v250
	v_mul_f32_e32 v230, 0x43800000, v178
	s_lshr_b32 s26, s53, 8
	v_cvt_pk_fp8_f32 v67, v226, v230 op_sel:[0,0,1]
	v_mul_f32_e32 v227, 0x43800000, v227
	v_mul_f32_e32 v230, 0x43800000, v231
	v_mov_b32_e32 v226, v83
	s_and_b32 s26, s26, 8
	v_mul_f32_e32 v231, 0x43800000, v235
	v_cvt_pk_fp8_f32 v226, v227, v230
	v_mul_f32_e32 v230, 0x43800000, v243
	v_mul_f32_e32 v235, 0x43800000, v247
	v_mov_b32_e32 v227, v83
	s_or_b32 s48, s50, s26
	s_lshl_b64 s[26:27], s[46:47], 12
	v_cvt_pk_fp8_f32 v227, v230, v235
	s_or_b32 s26, s26, s48
	v_mul_f32_e32 v234, 0x43800000, v234
	v_mul_f32_e32 v238, 0x43800000, v238
	s_waitcnt lgkmcnt(0)
	v_mov_b32_e32 v65, s27
	v_or_b32_e32 v64, s26, v80
	v_cvt_pk_fp8_f32 v66, v234, v238 op_sel:[0,0,1]
	v_mul_f32_e32 v234, 0x43800000, v239
	v_lshlrev_b64 v[64:65], 11, v[64:65]
	v_cvt_pk_fp8_f32 v226, v231, v234 op_sel:[0,0,1]
	v_mul_f32_e32 v230, 0x43800000, v251
	v_mul_f32_e32 v231, 0x43800000, v179
	v_lshl_add_u64 v[64:65], s[28:29], 0, v[64:65]
	v_cvt_pk_fp8_f32 v227, v230, v231 op_sel:[0,0,1]
	v_lshl_add_u64 v[230:231], v[64:65], 0, s[40:41]
	v_lshl_add_u64 v[230:231], v[230:231], 0, v[76:77]
	global_store_dwordx2 v[230:231], v[66:67], off
	global_store_dwordx2 v[230:231], v[226:227], off offset:2048
	v_mul_f32_e32 v227, 0x43800000, v228
	v_mul_f32_e32 v228, 0x43800000, v232
	v_mov_b32_e32 v226, v83
	v_cvt_pk_fp8_f32 v226, v227, v228
	v_mul_f32_e32 v228, 0x43800000, v244
	v_mul_f32_e32 v235, 0x43800000, v248
	v_mov_b32_e32 v227, v83
	v_cvt_pk_fp8_f32 v227, v228, v235
	v_mul_f32_e32 v232, 0x43800000, v236
	v_mul_f32_e32 v234, 0x43800000, v240
	v_cvt_pk_fp8_f32 v226, v232, v234 op_sel:[0,0,1]
	v_mul_f32_e32 v228, 0x43800000, v252
	v_mul_f32_e32 v232, 0x43800000, v180
	v_cvt_pk_fp8_f32 v227, v228, v232 op_sel:[0,0,1]
	v_mul_f32_e32 v229, 0x43800000, v229
	v_mul_f32_e32 v232, 0x43800000, v233
	v_mov_b32_e32 v228, v83
	v_cvt_pk_fp8_f32 v228, v229, v232
	v_mul_f32_e32 v232, 0x43800000, v245
	v_mul_f32_e32 v235, 0x43800000, v249
	v_mov_b32_e32 v229, v83
	v_cvt_pk_fp8_f32 v229, v232, v235
	v_mul_f32_e32 v233, 0x43800000, v237
	v_mul_f32_e32 v234, 0x43800000, v241
	v_cvt_pk_fp8_f32 v228, v233, v234 op_sel:[0,0,1]
	v_mul_f32_e32 v232, 0x43800000, v253
	v_mul_f32_e32 v233, 0x43800000, v181
	v_cvt_pk_fp8_f32 v229, v232, v233 op_sel:[0,0,1]
	v_add_co_u32_e32 v230, vcc, s72, v230
	v_add_u32_e32 v232, s49, v164
	s_nop 0
	v_addc_co_u32_e32 v231, vcc, 0, v231, vcc
	global_store_dwordx2 v[230:231], v[226:227], off
	global_store_dwordx2 v[230:231], v[228:229], off offset:2048
.Lp5dbl_noconsume:
	s_waitcnt lgkmcnt(0)
	s_barrier
	global_load_dword v40, v[84:85], off
	ds_read2st64_b32 v[32:33], v38 offset1:8
	ds_read2st64_b32 v[34:35], v38 offset0:16 offset1:24
	ds_read2st64_b32 v[36:37], v38 offset0:32 offset1:40
	ds_read2st64_b32 v[38:39], v38 offset0:48 offset1:56
	s_waitcnt vmcnt(0) lgkmcnt(3)
	v_add_f32_e32 v32, v40, v32
	v_add_f32_e32 v32, v32, v33
	s_waitcnt lgkmcnt(2)
	v_add_f32_e32 v32, v32, v34
	v_add_f32_e32 v32, v32, v35
	s_waitcnt lgkmcnt(1)
	v_add_f32_e32 v32, v32, v36
	v_add_f32_e32 v32, v32, v37
	s_waitcnt lgkmcnt(0)
	v_add_f32_e32 v32, v32, v38
	v_add_f32_e32 v34, v32, v39
	ds_bpermute_b32 v36, v157, v34
	ds_bpermute_b32 v37, v157, v163
	s_waitcnt lgkmcnt(1)
	v_cmp_lt_f32_e64 s[46:47], v34, v36
	v_cmp_nlt_f32_e32 vcc, v34, v36
	s_and_saveexec_b64 s[48:49], vcc
	s_cbranch_execz .LBB0_736
	v_cmp_eq_f32_e32 vcc, v34, v36
	s_waitcnt lgkmcnt(0)
	v_cmp_lt_i32_e64 s[26:27], v37, v163
	s_and_b64 s[26:27], vcc, s[26:27]
	s_andn2_b64 s[46:47], s[46:47], exec
	s_and_b64 s[26:27], s[26:27], exec
	s_or_b64 s[46:47], s[46:47], s[26:27]
